# v32 + DN fifth-round units cut into two 128-row halves on separate workgroups
# baseline (speedup 1.0000x reference)
; #define LAS __attribute__((address_space(3)))
; __device__ __forceinline__ int opaque_tid() { int t = threadIdx.x; asm volatile("" : "+v"(t)); return t; }
; __device__ __forceinline__ void seg_to_lds(const Args& a, LAS unsigned char* lds, int layer) {
;     LAS int* seg = (LAS int*)(lds + SEG_OFF);
;     const int t = opaque_tid();
;     if (t < 16) {
;         unsigned* cnt = (unsigned*)(a.ws + WS_CTL) + CW_CNT + layer * 16 * 64;
;         const int c = (int)__hip_atomic_load(cnt + t * 64, __ATOMIC_RELAXED, __HIP_MEMORY_SCOPE_AGENT);
;         const int pad = (c + 255) & ~255;
;         int incl = pad;
; #pragma unroll
;         for (int o2 = 1; o2 < 16; o2 <<= 1) { const int u2 = __shfl_up(incl, o2); if (t >= o2) incl += u2; }
;         seg[t] = c; seg[16 + t] = incl - pad;
;         if (t == 15) seg[32] = incl;
;     }
;     __syncthreads();
.Ldn_entry:
	s_mov_b32 s75, 0
	s_mov_b32 s78, 0
	v_mov_b32_e32 v1, v0
	s_waitcnt lgkmcnt(0)
	s_barrier
	s_nop 0
	v_cmp_gt_i32_e32 vcc, 0, v1
	s_and_saveexec_b64 s[4:5], vcc
	s_cbranch_execz .LBB0_1159
	v_lshlrev_b32_e32 v2, 6, v1
	v_readlane_b32 s6, v254, 22
	v_ashrrev_i32_e32 v3, 31, v2
	v_readlane_b32 s7, v254, 23
	v_cmp_lt_i32_e32 vcc, v235, v240
	s_nop 0
	v_lshl_add_u64 v[2:3], v[2:3], 2, s[6:7]
	global_load_dword v3, v[2:3], off sc1
	v_cndmask_b32_e32 v2, v235, v199, vcc
	v_lshlrev_b32_e32 v2, 2, v2
	v_cmp_lt_i32_e32 vcc, v233, v240
	s_waitcnt vmcnt(0)
	v_add_u32_e32 v4, 0xff, v3
	v_and_b32_e32 v4, 0xffffff00, v4
	ds_bpermute_b32 v2, v2, v4
	v_cndmask_b32_e32 v5, v233, v199, vcc
	v_cmp_lt_i32_e32 vcc, 0, v1
	v_lshlrev_b32_e32 v5, 2, v5
	s_waitcnt lgkmcnt(0)
	v_cndmask_b32_e32 v2, 0, v2, vcc
	v_add_u32_e32 v2, v4, v2
	ds_bpermute_b32 v5, v5, v2
	v_cmp_lt_i32_e32 vcc, v243, v240
	s_nop 1
	v_cndmask_b32_e32 v6, v243, v199, vcc
	v_cmp_lt_i32_e32 vcc, 1, v1
	v_lshlrev_b32_e32 v6, 2, v6
	s_waitcnt lgkmcnt(0)
	v_cndmask_b32_e32 v5, 0, v5, vcc
	v_add_u32_e32 v2, v2, v5
	ds_bpermute_b32 v5, v6, v2
	v_cmp_lt_i32_e32 vcc, v203, v240
	s_nop 1
	v_cndmask_b32_e32 v6, v203, v199, vcc
	v_cmp_lt_i32_e32 vcc, 3, v1
	v_lshlrev_b32_e32 v6, 2, v6
	s_waitcnt lgkmcnt(0)
	v_cndmask_b32_e32 v5, 0, v5, vcc
	v_add_u32_e32 v2, v2, v5
	ds_bpermute_b32 v5, v6, v2
	v_cmp_lt_i32_e32 vcc, 7, v1
	v_lshl_add_u32 v6, v1, 2, 0
	v_add_u32_e32 v6, 0x21e00, v6
	s_waitcnt lgkmcnt(0)
	v_cndmask_b32_e32 v5, 0, v5, vcc
	v_add_u32_e32 v2, v2, v5
	v_sub_u32_e32 v4, v2, v4
	v_cmp_eq_u32_e32 vcc, 15, v1
	ds_write2_b32 v6, v3, v4 offset1:16
	s_and_b64 exec, exec, vcc
	s_cbranch_execz .LBB0_1159
	v_readlane_b32 s2, v253, 58
	s_nop 1
	v_mov_b32_e32 v1, s2
	ds_write_b32 v1, v2

; #define LAS __attribute__((address_space(3)))
; #define PG8_BAR __builtin_amdgcn_s_barrier()
; #define PG8_BAR __builtin_amdgcn_s_barrier()
;     ...
;         for (int a = 0; a < 2; ++a)
; #pragma unroll
;             for (int b = 0; b < 2; ++b)
; #pragma unroll
;                 for (int m = 0; m < 4; ++m)
; #pragma unroll
;                     for (int n = 0; n < 2; ++n) acc[a][b][m][n] = (f32x4){0.f, 0.f, 0.f, 0.f};
;         cur = nxt; cA = nA; cB = nB; ++ui;
;         if (wr == 1) PG8_BAR;
;     __device__ __forceinline__ void pre(LAS unsigned char* lds, const pg8::Unit& u, int tid) const {
;         const int t = tid & 255, wv = __builtin_amdgcn_readfirstlane(tid >> 6);
;         const void* src = tid < 256 ? (const void*)(list + u.e * NTOK + u.pm * 256 + t) : (const void*)(listw + u.e * NTOK + u.pm * 256 + t);
;         lds_dma4(src, (unsigned)__builtin_amdgcn_readfirstlane((unsigned)(uintptr_t)lds + DNSL_OFF + u.par * 2048 + wv * 256));
;     }
.LBB0_1225:
	v_mov_b32_e32 v34, v35
	v_mov_b32_e32 v36, v35
	v_mov_b32_e32 v37, v35
	v_mov_b32_e32 v70, 0
	v_mov_b64_e32 v[2:3], v[34:35]
	v_mov_b64_e32 v[6:7], v[34:35]
	v_mov_b64_e32 v[10:11], v[34:35]
	v_mov_b64_e32 v[14:15], v[34:35]
	v_mov_b64_e32 v[18:19], v[34:35]
	v_mov_b64_e32 v[22:23], v[34:35]
	v_mov_b64_e32 v[26:27], v[34:35]
	v_mov_b64_e32 v[30:31], v[34:35]
	v_mov_b64_e32 v[40:41], v[36:37]
	v_mov_b64_e32 v[44:45], v[36:37]
	v_mov_b64_e32 v[48:49], v[36:37]
	v_mov_b64_e32 v[52:53], v[36:37]
	v_mov_b64_e32 v[56:57], v[36:37]
	v_mov_b64_e32 v[60:61], v[36:37]
	v_mov_b64_e32 v[64:65], v[36:37]
	v_mov_b64_e32 v[68:69], v[36:37]
	v_mov_b64_e32 v[4:5], v[36:37]
	v_mov_b64_e32 v[8:9], v[36:37]
	v_mov_b64_e32 v[12:13], v[36:37]
	v_mov_b64_e32 v[16:17], v[36:37]
	v_mov_b64_e32 v[20:21], v[36:37]
	v_mov_b64_e32 v[24:25], v[36:37]
	v_mov_b64_e32 v[28:29], v[36:37]
	v_mov_b64_e32 v[32:33], v[36:37]
	v_mov_b64_e32 v[38:39], v[34:35]
	v_mov_b64_e32 v[42:43], v[34:35]
	v_mov_b64_e32 v[46:47], v[34:35]
	v_mov_b64_e32 v[50:51], v[34:35]
	v_mov_b64_e32 v[54:55], v[34:35]
	v_mov_b64_e32 v[58:59], v[34:35]
	v_mov_b64_e32 v[62:63], v[34:35]
	v_mov_b64_e32 v[66:67], v[34:35]
	v_mov_b32_e32 v203, v246
	s_mov_b32 s10, s21
	s_mov_b32 s12, s20
	s_mov_b32 s41, s48
	s_mov_b32 s78, s75
	s_cmp_eq_u32 s78, 0
	s_cbranch_scc1 .Ldn_st1
	v_min_i32_e32 v203, 0x80, v203
.Ldn_st1:
	v_mov_b32_e32 v71, v70
	v_mov_b32_e32 v72, v70
	v_mov_b32_e32 v73, v70
	v_mov_b32_e32 v74, v70
	v_mov_b32_e32 v75, v70
	v_mov_b32_e32 v76, v70
	v_mov_b32_e32 v77, v70
	v_mov_b32_e32 v78, v70
	v_mov_b32_e32 v79, v70
	v_mov_b32_e32 v80, v70
	v_mov_b32_e32 v81, v70
	v_mov_b32_e32 v82, v70
	v_mov_b32_e32 v83, v70
	v_mov_b32_e32 v84, v70
	v_mov_b32_e32 v85, v70
	v_mov_b32_e32 v86, v70
	v_mov_b32_e32 v87, v70
	v_mov_b32_e32 v88, v70
	v_mov_b32_e32 v89, v70
	v_mov_b32_e32 v90, v70
	v_mov_b32_e32 v91, v70
	v_mov_b32_e32 v92, v70
	v_mov_b32_e32 v93, v70
	v_mov_b32_e32 v94, v70
	v_mov_b32_e32 v95, v70
	v_mov_b32_e32 v96, v70
	v_mov_b32_e32 v97, v70
	v_mov_b32_e32 v98, v70
	v_mov_b32_e32 v99, v70
	v_mov_b32_e32 v100, v70
	v_mov_b32_e32 v101, v70
	v_mov_b32_e32 v102, v70
	v_mov_b32_e32 v103, v70
	v_mov_b32_e32 v104, v70
	v_mov_b32_e32 v105, v70
	v_mov_b32_e32 v106, v70
	v_mov_b32_e32 v107, v70
	v_mov_b32_e32 v108, v70
	v_mov_b32_e32 v109, v70
	v_mov_b32_e32 v110, v70
	v_mov_b32_e32 v111, v70
	v_mov_b32_e32 v112, v70
	v_mov_b32_e32 v113, v70
	v_mov_b32_e32 v114, v70
	v_mov_b32_e32 v115, v70
	v_mov_b32_e32 v116, v70
	v_mov_b32_e32 v117, v70
	v_mov_b32_e32 v118, v70
	v_mov_b32_e32 v119, v70
	v_mov_b32_e32 v120, v70
	v_mov_b32_e32 v121, v70
	v_mov_b32_e32 v122, v70
	v_mov_b32_e32 v123, v70
	v_mov_b32_e32 v124, v70
	v_mov_b32_e32 v125, v70
	v_mov_b32_e32 v126, v70
	v_mov_b32_e32 v127, v70
	v_mov_b32_e32 v128, v70
	v_mov_b32_e32 v129, v70
	v_mov_b32_e32 v130, v70
	v_mov_b32_e32 v131, v70
	v_mov_b32_e32 v132, v70
	v_mov_b32_e32 v133, v70
	s_mov_b64 s[14:15], s[28:29]
	s_mov_b32 s49, s23
	s_andn2_b64 vcc, exec, s[24:25]
	s_mov_b64 s[6:7], s[26:27]
	s_cbranch_vccz .LBB0_1320
.LBB0_1226:
	s_lshl_b32 s8, s10, 15
	s_lshl_b32 s22, s41, 8
	s_cmp_eq_u32 s78, 2
	s_cbranch_scc0 .Ldn_sl1
	s_addk_i32 s22, 0x80
.Ldn_sl1:
	v_readfirstlane_b32 s26, v1
	s_ashr_i32 s9, s8, 31
	s_ashr_i32 s23, s22, 31
	v_lshlrev_b32_e32 v34, 2, v200
	s_and_saveexec_b64 s[24:25], s[4:5]
	s_xor_b64 s[24:25], exec, s[24:25]
	s_cbranch_execz .LBB0_1228
	s_lshl_b64 s[28:29], s[8:9], 2
	v_readlane_b32 s30, v253, 25
	v_readlane_b32 s31, v253, 26
	s_add_u32 s27, s30, s28
	s_addc_u32 s30, s31, s29
	s_lshl_b64 s[28:29], s[22:23], 2
	s_add_u32 s28, s27, s28
	s_addc_u32 s29, s30, s29
	v_lshl_add_u64 v[36:37], s[28:29], 0, v[34:35]

; #define LAS __attribute__((address_space(3)))
;     __device__ __forceinline__ bool next(int i, Unit& u) const {
;         int U = i * G + c, e = 0, found = 0, rem = 0;
;         typedef int i32x4 __attribute__((ext_vector_type(4)));
;         const i32x4 c0 = *(const LAS i32x4*)(seg), c1 = *(const LAS i32x4*)(seg + 4), c2 = *(const LAS i32x4*)(seg + 8), c3 = *(const LAS i32x4*)(seg + 12);
; #pragma unroll
;         for (int k = 0; k < 16; ++k) { const int ck = k < 4 ? c0[k & 3] : k < 8 ? c1[k & 3] : k < 12 ? c2[k & 3] : c3[k & 3];
;             const int nu = ((ck + 255) >> 8) * nct; if (!found) { if (U < nu) { found = 1; e = k; rem = U; } else U -= nu; } }
;     __device__ __forceinline__ void pre(LAS unsigned char* lds, const pg8::Unit& u, int tid) const {
;     ...
;         const void* src = tid < 256 ? (const void*)(list + u.e * NTOK + u.pm * 256 + t) : (const void*)(listw + u.e * NTOK + u.pm * 256 + t);
;         lds_dma4(src, (unsigned)__builtin_amdgcn_readfirstlane((unsigned)(uintptr_t)lds + DNSL_OFF + u.par * 2048 + wv * 256));
.LBB0_1230:
	s_or_b64 exec, exec, s[24:25]
	s_lshl_b32 s8, s49, 11
	s_and_b32 s8, s8, 0x800
	s_lshl_b32 s9, s26, 2
	s_and_b32 s9, s9, 0xffffff00
	s_add_i32 s54, s8, 0
	s_add_i32 s8, s54, s9
	s_add_i32 s8, s8, 0x22400
	s_mov_b32 s9, m0
	s_mov_b32 m0, s8
	s_nop 0
	global_load_lds_dword v[36:37], off
	s_mov_b32 m0, s9
	v_mov_b32_e32 v34, s42
	ds_read_b128 v[134:137], v34
	s_add_i32 s23, s49, 1
	s_mul_i32 s8, s23, s77
	s_add_i32 s9, s8, s61
	s_mov_b32 s75, 0
	s_cmp_lt_u32 s23, 3
	s_cbranch_scc1 .Ldn_perm_done
	v_readlane_b32 s24, v254, 63
	s_nop 1
	s_cmp_lt_u32 s61, s24
	s_cbranch_scc1 .Ldn_perm_bad
	s_sub_i32 s25, s77, s24
	s_add_i32 s26, s23, -3
	s_mul_i32 s25, s25, s26
	s_sub_i32 s26, s61, s24
	s_cmp_eq_u32 s23, 4
	s_cbranch_scc0 .Ldn_half_skip
	s_and_b32 s75, s26, 1
	s_add_i32 s75, s75, 1
	s_lshr_b32 s26, s26, 1
.Ldn_half_skip:
	s_add_i32 s25, s25, s26
	s_mul_i32 s26, s77, 3
	s_add_i32 s9, s25, s26
	s_lshl_b32 s26, s77, 2
	s_cmp_lt_u32 s9, s26
	s_cbranch_scc1 .Ldn_perm_done
	s_add_i32 s26, s26, s24
	s_cmp_ge_u32 s9, s26
	s_cbranch_scc1 .Ldn_perm_done
	v_readlane_b32 s27, v254, 20
	s_nop 1
	s_lshl_b32 s27, s27, 2
	s_add_u32 s27, s27, 0x18000
	s_add_u32 s28, s92, s27
	s_addc_u32 s29, s93, 0
	v_mov_b32_e32 v138, 0
	s_mov_b32 s30, 0

;     __device__ __forceinline__ bool next(int i, Unit& u) const {
;     ...
;         e = __builtin_amdgcn_readfirstlane(e); rem = __builtin_amdgcn_readfirstlane(rem);
;         const int rt = rem / nct, ct = rem % nct;
;         u.e = e; u.pm = rt; u.pn = ct; u.rows = seg[e] - rt * 256;
;         u.a = A + (size_t)(seg[16 + e] + rt * 256) * arow_bytes; u.b = Bt + (size_t)e * bexp_bytes + (size_t)ct * btile_bytes; return true;
.LBB0_1290:
	s_xor_b64 s[24:25], s[30:31], -1
	s_and_b64 vcc, exec, s[24:25]
	s_mov_b64 s[26:27], s[6:7]
	s_mov_b64 s[28:29], s[14:15]
	s_cbranch_vccnz .LBB0_1292
	s_lshl_b32 s21, s8, 2
	s_add_i32 s21, s21, 0
	s_add_i32 s21, s21, 0x21e00
	v_mov_b32_e32 v34, s21
	ds_read2_b32 v[36:37], v34 offset1:16
	s_ashr_i32 s20, s9, 31
	s_lshr_b32 s20, s20, 30
	s_add_i32 s20, s9, s20
	s_ashr_i32 s48, s20, 2
	s_lshl_b32 s21, s48, 8
	s_cmp_eq_u32 s75, 2
	s_cbranch_scc0 .Ldn_sd1
	s_addk_i32 s21, 0x80
.Ldn_sd1:
	s_waitcnt lgkmcnt(0)
	v_readfirstlane_b32 s26, v37
	s_add_i32 s26, s26, s21
	s_and_b32 s20, s20, -4
	s_ashr_i32 s27, s26, 31
	s_sub_i32 s20, s9, s20
	s_ashr_i32 s9, s8, 31
	s_lshl_b64 s[26:27], s[26:27], 10
	v_readlane_b32 s28, v253, 29
	v_readlane_b32 s29, v253, 30
	s_add_u32 s28, s28, s26
	s_addc_u32 s29, s29, s27
	s_lshl_b64 s[26:27], s[8:9], 20
	s_add_u32 s9, s2, s26
	v_subrev_u32_e32 v246, s21, v36
	s_addc_u32 s33, s40, s27
	s_ashr_i32 s21, s20, 31
	s_lshl_b64 s[26:27], s[20:21], 18
	s_add_u32 s26, s9, s26
	s_addc_u32 s27, s33, s27
	s_mov_b32 s21, s8

; #define LAS __attribute__((address_space(3)))
; __device__ __forceinline__ unsigned cvt_pk_bf16(float lo, float hi) { unsigned r; asm volatile("v_cvt_pk_bf16_f32 %0, %1, %2" : "=v"(r) : "v"(lo), "v"(hi)); return r; }
;     __device__ __forceinline__ void operator()(const f32x4 (&acc)[2][2][4][2], const pg8::Unit& u, int wr, int wc, int fr, int fq) const {
;         const int cnt = seg[u.e], col0 = u.pn * 256 + wc * 32 + 8 * fq;
;         const LAS int* sl_e = (const LAS int*)(ldsb + DNSL_OFF + u.par * 2048); const LAS float* sl_g = (const LAS float*)(ldsb + DNSL_OFF + u.par * 2048 + 1024);
; #pragma unroll
;         for (int ai = 0; ai < 2; ++ai)
; #pragma unroll
;             for (int m = 0; m < 4; ++m) {
;                 const int ll = ai * 128 + wr * 64 + m * 16 + fr, lr = u.pm * 256 + ll;
;                 if (lr < cnt) {
;                     const int ent = sl_e[ll]; const float gw = sl_g[ll];
;                     bf16_t* rowp = yb + ((size_t)(ent & 1) * NTOK + (size_t)(ent >> 1)) * D + col0;
; #pragma unroll
;                     for (int bj = 0; bj < 2; ++bj) {
;                         const f32x4 v0 = acc[ai][bj][m][0] * gw, v1 = acc[ai][bj][m][1] * gw;
;                         u32x4 w; w.x = pg8::cvt_pk_bf16(v0[0], v0[1]); w.y = pg8::cvt_pk_bf16(v0[2], v0[3]); w.z = pg8::cvt_pk_bf16(v1[0], v1[1]); w.w = pg8::cvt_pk_bf16(v1[2], v1[3]);
;                         *(u32x4*)(rowp + bj * 128) = w;
.LBB0_1300:
	s_lshl_b32 s6, s10, 2
	s_add_i32 s6, s6, 0
	s_add_i32 s6, s6, 0x21e00
	v_mov_b32_e32 v34, s6
	ds_read_b32 v134, v34
	v_lshl_or_b32 v36, s12, 8, v244
	s_add_i32 s54, s54, 0x22400
	v_add_u32_e32 v136, s22, v226
	v_ashrrev_i32_e32 v37, 31, v36
	s_waitcnt lgkmcnt(0)
	s_cmp_eq_u32 s78, 0
	s_cbranch_scc1 .Ldn_se1
	s_add_i32 s79, s22, 0x80
	v_min_i32_e32 v134, s79, v134
.Ldn_se1:
	v_cmp_lt_i32_e32 vcc, v136, v134
	v_lshl_add_u32 v135, v226, 2, s54
	s_and_saveexec_b64 s[6:7], vcc
	s_cbranch_execz .LBB0_1302
	ds_read2st64_b32 v[138:139], v135 offset1:4
	s_waitcnt lgkmcnt(0)
	v_lshlrev_b32_e32 v34, 15, v138
	v_ashrrev_i32_e32 v138, 1, v138
	v_mov_b32_e32 v142, v139
	v_and_b32_e32 v34, 0x8000, v34
	v_ashrrev_i32_e32 v139, 31, v138
	v_lshl_add_u64 v[138:139], v[34:35], 0, v[138:139]
	v_lshlrev_b64 v[138:139], 11, v[138:139]
	v_lshl_add_u64 v[138:139], s[96:97], 0, v[138:139]
	v_pk_mul_f32 v[140:141], v[132:133], v[142:143] op_sel_hi:[1,0]
	v_lshl_add_u64 v[144:145], v[36:37], 1, v[138:139]
	v_pk_mul_f32 v[138:139], v[130:131], v[142:143] op_sel_hi:[1,0]
	v_pk_mul_f32 v[146:147], v[128:129], v[142:143] op_sel_hi:[1,0]
	v_pk_mul_f32 v[148:149], v[126:127], v[142:143] op_sel_hi:[1,0]
	v_cvt_pk_bf16_f32 v138, v138, v139
	v_cvt_pk_bf16_f32 v139, v140, v141
	s_nop 0
	v_cvt_pk_bf16_f32 v140, v148, v149
	v_cvt_pk_bf16_f32 v141, v146, v147
	global_store_dwordx4 v[144:145], v[138:141], off
	v_pk_mul_f32 v[146:147], v[96:97], v[142:143] op_sel_hi:[1,0]
	s_nop 0
	v_pk_mul_f32 v[140:141], v[100:101], v[142:143] op_sel_hi:[1,0]
	v_pk_mul_f32 v[138:139], v[98:99], v[142:143] op_sel_hi:[1,0]
	v_pk_mul_f32 v[142:143], v[94:95], v[142:143] op_sel_hi:[1,0]
	v_cvt_pk_bf16_f32 v138, v138, v139
	v_cvt_pk_bf16_f32 v139, v140, v141
	s_nop 0
	v_cvt_pk_bf16_f32 v140, v142, v143
	v_cvt_pk_bf16_f32 v141, v146, v147
	global_store_dwordx4 v[144:145], v[138:141], off offset:256
